# attn_fox QK: second batch's LDS reads issued behind the first batch's MFMAs, counted lgkmcnt waits, on top of v90
# speedup vs baseline: 1.0010x; 1.0010x over previous
.LBB0_522:
	v_add_u32_e32 v2, s14, v220
	v_mad_i64_i32 v[4:5], s[12:13], v2, s24, v[200:201]
	v_add_u32_e32 v2, s14, v219
	v_mad_i64_i32 v[6:7], s[12:13], v2, s24, v[200:201]
	v_add_u32_e32 v2, s14, v218
	global_load_dwordx4 v[8:11], v[204:205], off
	global_load_dwordx4 v[114:117], v[4:5], off
	global_load_dwordx4 v[12:15], v[6:7], off
	s_nop 0
	global_load_dwordx4 v[4:7], v[202:203], off
	v_lshl_add_u64 v[16:17], v[2:3], 2, s[10:11]
	global_load_dword v2, v[16:17], off
	s_cmp_gt_i32 s14, s19
	s_cbranch_scc1 .LBB0_528
	s_bitcmp1_b32 s20, 0
	s_cselect_b32 s12, 0, 0x8900
	s_add_i32 s12, s72, s12
	v_add3_u32 v16, s12, v217, v196
	ds_read_b128 v[82:85], v16
	ds_read_b128 v[118:121], v16 offset:32
	ds_read_b128 v[86:89], v16 offset:8704
	ds_read_b128 v[122:125], v16 offset:8736
	ds_read_b128 v[126:129], v16 offset:64
	ds_read_b128 v[130:133], v16 offset:96
	ds_read_b128 v[134:137], v16 offset:8768
	ds_read_b128 v[138:141], v16 offset:8800
	s_waitcnt lgkmcnt(7)
	v_mfma_f32_32x32x16_bf16 v[98:113], v[82:85], v[174:177], 0
	s_waitcnt lgkmcnt(5)
	v_mfma_f32_32x32x16_bf16 v[82:97], v[86:89], v[174:177], 0
	v_mfma_f32_32x32x16_bf16 v[98:113], v[118:121], v[170:173], v[98:113]
	ds_read_b128 v[118:121], v16 offset:128
	s_waitcnt lgkmcnt(5)
	v_mfma_f32_32x32x16_bf16 v[82:97], v[122:125], v[170:173], v[82:97]
	ds_read_b128 v[122:125], v16 offset:160
	s_waitcnt lgkmcnt(5)
	v_mfma_f32_32x32x16_bf16 v[98:113], v[126:129], v[166:169], v[98:113]
	ds_read_b128 v[126:129], v16 offset:8832
	s_waitcnt lgkmcnt(4)
	v_mfma_f32_32x32x16_bf16 v[82:97], v[134:137], v[166:169], v[82:97]
	ds_read_b128 v[134:137], v16 offset:192
	v_mfma_f32_32x32x16_bf16 v[98:113], v[130:133], v[162:165], v[98:113]
	ds_read_b128 v[130:133], v16 offset:8864
	s_waitcnt lgkmcnt(5)
	v_mfma_f32_32x32x16_bf16 v[82:97], v[138:141], v[162:165], v[82:97]
	ds_read_b128 v[138:141], v16 offset:8896
	ds_read_b128 v[142:145], v16 offset:224
	ds_read_b128 v[182:185], v16 offset:8928
	s_waitcnt lgkmcnt(7)
	v_mfma_f32_32x32x16_bf16 v[98:113], v[118:121], v[158:161], v[98:113]
	v_add_u32_e32 v16, s12, v199
	v_add_u32_e32 v221, v16, v197
	v_add_u32_e32 v16, 0x4000, v221
	s_waitcnt lgkmcnt(5)
	v_mfma_f32_32x32x16_bf16 v[82:97], v[126:129], v[158:161], v[82:97]
	v_mfma_f32_32x32x16_bf16 v[98:113], v[122:125], v[154:157], v[98:113]
	s_waitcnt lgkmcnt(3)
	v_mfma_f32_32x32x16_bf16 v[82:97], v[130:133], v[154:157], v[82:97]
	v_mfma_f32_32x32x16_bf16 v[98:113], v[134:137], v[150:153], v[98:113]
	s_waitcnt lgkmcnt(0)
	v_mfma_f32_32x32x16_bf16 v[82:97], v[138:141], v[150:153], v[82:97]
	ds_read2_b64 v[178:181], v16 offset0:128 offset1:130
	ds_read2_b64 v[138:141], v16 offset0:132 offset1:134
	v_mfma_f32_32x32x16_bf16 v[98:113], v[142:145], v[146:149], v[98:113]
	ds_read2_b64 v[142:145], v16 offset0:136 offset1:138
	ds_read2_b64 v[134:137], v16 offset0:140 offset1:142
	v_add_u32_e32 v16, 0x5000, v221
	ds_read2_b64 v[130:133], v16 offset0:160 offset1:162
	ds_read2_b64 v[126:129], v16 offset0:164 offset1:166
	ds_read2_b64 v[122:125], v16 offset0:168 offset1:170
	ds_read2_b64 v[118:121], v16 offset0:172 offset1:174
	v_mfma_f32_32x32x16_bf16 v[82:97], v[182:185], v[146:149], v[82:97]
	v_lshl_add_u32 v16, v1, 2, s12
	ds_read_b128 v[182:185], v16 offset:34816
	ds_read_b128 v[186:189], v16 offset:34848
	ds_read_b128 v[222:225], v16 offset:34944
	ds_read_b128 v[232:235], v16 offset:34976
	ds_read_b128 v[236:239], v16 offset:34880
	ds_read_b128 v[242:245], v16 offset:34912
	ds_read_b128 v[246:249], v16 offset:35008
	ds_read_b128 v[190:193], v16 offset:35040
	s_add_i32 s13, s14, 63
	s_waitcnt lgkmcnt(0)
	v_xor_b32_e32 v185, 0x80000000, v185
	v_xor_b32_e32 v184, 0x80000000, v184
	v_xor_b32_e32 v17, 0x80000000, v245
	v_xor_b32_e32 v16, 0x80000000, v244
	s_mov_b32 s12, 0x3e0293ee
	v_xor_b32_e32 v189, 0x80000000, v189
	v_xor_b32_e32 v188, 0x80000000, v188
	v_xor_b32_e32 v239, 0x80000000, v239
	v_xor_b32_e32 v238, 0x80000000, v238
	v_pk_fma_f32 v[206:207], v[102:103], s[12:13], v[186:187] op_sel_hi:[1,0,1] neg_lo:[0,0,1] neg_hi:[0,0,1]
	v_pk_fma_f32 v[16:17], v[112:113], s[12:13], v[16:17] op_sel_hi:[1,0,1]
	v_pk_fma_f32 v[100:101], v[100:101], s[12:13], v[184:185] op_sel_hi:[1,0,1]
	v_pk_fma_f32 v[98:99], v[98:99], s[12:13], v[182:183] op_sel_hi:[1,0,1] neg_lo:[0,0,1] neg_hi:[0,0,1]
	v_xor_b32_e32 v113, 0x80000000, v225
	v_xor_b32_e32 v112, 0x80000000, v224
	v_xor_b32_e32 v183, 0x80000000, v235
	v_xor_b32_e32 v182, 0x80000000, v234
	v_xor_b32_e32 v185, 0x80000000, v249
	v_xor_b32_e32 v184, 0x80000000, v248
	v_xor_b32_e32 v187, 0x80000000, v193
	v_xor_b32_e32 v186, 0x80000000, v192
	v_pk_fma_f32 v[110:111], v[110:111], s[12:13], v[242:243] op_sel_hi:[1,0,1] neg_lo:[0,0,1] neg_hi:[0,0,1]
	v_pk_fma_f32 v[106:107], v[106:107], s[12:13], v[236:237] op_sel_hi:[1,0,1] neg_lo:[0,0,1] neg_hi:[0,0,1]
	v_pk_fma_f32 v[102:103], v[108:109], s[12:13], v[238:239] op_sel_hi:[1,0,1]
	v_pk_fma_f32 v[104:105], v[104:105], s[12:13], v[188:189] op_sel_hi:[1,0,1]
	v_pk_fma_f32 v[94:95], v[94:95], s[12:13], v[190:191] op_sel_hi:[1,0,1] neg_lo:[0,0,1] neg_hi:[0,0,1]
	v_pk_fma_f32 v[90:91], v[90:91], s[12:13], v[246:247] op_sel_hi:[1,0,1] neg_lo:[0,0,1] neg_hi:[0,0,1]
	v_pk_fma_f32 v[108:109], v[86:87], s[12:13], v[232:233] op_sel_hi:[1,0,1] neg_lo:[0,0,1] neg_hi:[0,0,1]
	v_pk_fma_f32 v[86:87], v[96:97], s[12:13], v[186:187] op_sel_hi:[1,0,1]
	v_pk_fma_f32 v[92:93], v[92:93], s[12:13], v[184:185] op_sel_hi:[1,0,1]
	v_pk_fma_f32 v[88:89], v[88:89], s[12:13], v[182:183] op_sel_hi:[1,0,1]
	v_pk_fma_f32 v[84:85], v[84:85], s[12:13], v[112:113] op_sel_hi:[1,0,1]
	s_cmp_le_i32 s13, s18
	v_pk_fma_f32 v[82:83], v[82:83], s[12:13], v[222:223] op_sel_hi:[1,0,1] neg_lo:[0,0,1] neg_hi:[0,0,1]
	s_cbranch_scc1 .LBB0_525
	v_add_u32_e32 v96, s14, v1
	v_add_u32_e32 v97, 32, v96
	v_cmp_le_i32_e32 vcc, v97, v211
	v_add_u32_e32 v97, 33, v96
	s_nop 0
	v_cndmask_b32_e32 v82, v229, v82, vcc
	v_cmp_lt_i32_e32 vcc, v96, v211
	s_nop 1
	v_cndmask_b32_e32 v99, v229, v99, vcc
	v_cmp_le_i32_e32 vcc, v96, v211
	s_nop 1
	v_cndmask_b32_e32 v98, v229, v98, vcc
	v_cmp_le_i32_e32 vcc, v97, v211
	v_add_u32_e32 v97, 2, v96
	s_nop 0
	v_cndmask_b32_e32 v83, v229, v83, vcc
	v_cmp_le_i32_e32 vcc, v97, v211
	v_add_u32_e32 v97, 34, v96
	s_nop 0
	v_cndmask_b32_e32 v100, v229, v100, vcc
	v_cmp_le_i32_e32 vcc, v97, v211
	v_add_u32_e32 v97, 3, v96
	s_nop 0
	v_cndmask_b32_e32 v84, v229, v84, vcc
	v_cmp_le_i32_e32 vcc, v97, v211
	v_add_u32_e32 v97, 35, v96
	s_nop 0
	v_cndmask_b32_e32 v101, v229, v101, vcc
	v_cmp_le_i32_e32 vcc, v97, v211
	v_add_u32_e32 v97, 8, v96
	s_nop 0
	v_cndmask_b32_e32 v85, v229, v85, vcc
	v_cmp_le_i32_e32 vcc, v97, v211
	v_add_u32_e32 v97, 40, v96
	s_nop 0
	v_cndmask_b32_e32 v206, v229, v206, vcc
	v_cmp_le_i32_e32 vcc, v97, v211
	v_add_u32_e32 v97, 9, v96
	s_nop 0
	v_cndmask_b32_e32 v108, v229, v108, vcc
	v_cmp_le_i32_e32 vcc, v97, v211
	v_add_u32_e32 v97, 41, v96
	s_nop 0
	v_cndmask_b32_e32 v207, v229, v207, vcc
	v_cmp_le_i32_e32 vcc, v97, v211
	v_add_u32_e32 v97, 10, v96
	s_nop 0
	v_cndmask_b32_e32 v109, v229, v109, vcc
	v_cmp_le_i32_e32 vcc, v97, v211
	v_add_u32_e32 v97, 42, v96
	s_nop 0
	v_cndmask_b32_e32 v104, v229, v104, vcc
	v_cmp_le_i32_e32 vcc, v97, v211
	v_add_u32_e32 v97, 11, v96
	s_nop 0
	v_cndmask_b32_e32 v88, v229, v88, vcc
	v_cmp_le_i32_e32 vcc, v97, v211
	v_add_u32_e32 v97, 43, v96
	s_nop 0
	v_cndmask_b32_e32 v105, v229, v105, vcc
	v_cmp_le_i32_e32 vcc, v97, v211
	v_add_u32_e32 v97, 16, v96
	s_nop 0
	v_cndmask_b32_e32 v89, v229, v89, vcc
	v_cmp_le_i32_e32 vcc, v97, v211
	v_add_u32_e32 v97, 48, v96
	s_nop 0
	v_cndmask_b32_e32 v106, v229, v106, vcc
	v_cmp_le_i32_e32 vcc, v97, v211
	v_add_u32_e32 v97, 17, v96
	s_nop 0
	v_cndmask_b32_e32 v90, v229, v90, vcc
	v_cmp_le_i32_e32 vcc, v97, v211
	v_add_u32_e32 v97, 49, v96
	s_nop 0
	v_cndmask_b32_e32 v107, v229, v107, vcc
	v_cmp_le_i32_e32 vcc, v97, v211
	v_add_u32_e32 v97, 18, v96
	s_nop 0
	v_cndmask_b32_e32 v91, v229, v91, vcc
	v_cmp_le_i32_e32 vcc, v97, v211
	v_add_u32_e32 v97, 50, v96
	s_nop 0
	v_cndmask_b32_e32 v102, v229, v102, vcc
	v_cmp_le_i32_e32 vcc, v97, v211
	v_add_u32_e32 v97, 19, v96
	s_nop 0
	v_cndmask_b32_e32 v92, v229, v92, vcc
	v_cmp_le_i32_e32 vcc, v97, v211
	v_add_u32_e32 v97, 51, v96
	s_nop 0
	v_cndmask_b32_e32 v103, v229, v103, vcc
	v_cmp_le_i32_e32 vcc, v97, v211
	v_add_u32_e32 v97, 24, v96
	s_nop 0
	v_cndmask_b32_e32 v93, v229, v93, vcc
	v_cmp_le_i32_e32 vcc, v97, v211
	v_add_u32_e32 v97, 56, v96
	s_nop 0
	v_cndmask_b32_e32 v110, v229, v110, vcc
	v_cmp_le_i32_e32 vcc, v97, v211
	v_add_u32_e32 v97, 25, v96
	s_nop 0
	v_cndmask_b32_e32 v94, v229, v94, vcc
	v_cmp_le_i32_e32 vcc, v97, v211
	v_add_u32_e32 v97, 57, v96
	s_nop 0
	v_cndmask_b32_e32 v111, v229, v111, vcc
	v_cmp_le_i32_e32 vcc, v97, v211
	v_add_u32_e32 v97, 26, v96
	s_nop 0
	v_cndmask_b32_e32 v95, v229, v95, vcc
	v_cmp_le_i32_e32 vcc, v97, v211
	v_add_u32_e32 v97, 58, v96
	s_nop 0
	v_cndmask_b32_e32 v16, v229, v16, vcc
	v_cmp_le_i32_e32 vcc, v97, v211
	v_add_u32_e32 v97, 27, v96
	v_add_u32_e32 v96, 59, v96
	v_cndmask_b32_e32 v86, v229, v86, vcc
	v_cmp_le_i32_e32 vcc, v97, v211
	s_nop 1
	v_cndmask_b32_e32 v17, v229, v17, vcc
	v_cmp_le_i32_e32 vcc, v96, v211
	s_nop 1
	v_cndmask_b32_e32 v87, v229, v87, vcc
